# q6 + phase G: LN2 gamma/beta staged once per phase in LDS instead of 16 global loads + 4 full vmcnt(0) round trips per token
# speedup vs baseline: 1.0220x; 1.0220x over previous
.LBB0_2903:
	s_or_b64 exec, exec, s[14:15]
	s_andn2_b64 vcc, exec, s[12:13]
	s_cbranch_vccnz .LBB0_2918
	s_cmp_eq_u32 s36, 3
	s_mov_b64 s[14:15], s[70:71]
	s_cselect_b32 s17, s15, 0
	s_cselect_b32 s16, s14, 0
	s_lshl_b32 s12, s37, 13
	v_lshlrev_b32_e32 v2, 3, v102
	s_add_i32 s14, s12, 0
	v_lshl_add_u64 v[4:5], s[6:7], 0, v[2:3]
	s_mov_b64 s[12:13], 0x4fb00000
	v_and_b32_e32 v2, 64, v219
	v_lshl_add_u64 v[14:15], v[4:5], 0, s[12:13]
	v_add_u32_e32 v2, 64, v2
	v_xor_b32_e32 v4, 1, v219
	v_cmp_lt_i32_e32 vcc, v4, v2
	s_lshl_b32 s18, s36, 11
	s_ashr_i32 s19, s18, 31
	v_cndmask_b32_e32 v4, v219, v4, vcc
	v_lshlrev_b32_e32 v104, 2, v4
	v_xor_b32_e32 v4, 2, v219
	v_cmp_lt_i32_e32 vcc, v4, v2
	s_cmp_lg_u64 s[16:17], 0
	s_mov_b64 s[20:21], 0x4ae00000
	v_cndmask_b32_e32 v4, v219, v4, vcc
	v_lshlrev_b32_e32 v105, 2, v4
	v_xor_b32_e32 v4, 4, v219
	v_cmp_lt_i32_e32 vcc, v4, v2
	v_lshl_add_u32 v103, v102, 5, s14
	s_cselect_b64 s[12:13], -1, 0
	v_cndmask_b32_e32 v4, v219, v4, vcc
	v_lshlrev_b32_e32 v106, 2, v4
	v_xor_b32_e32 v4, 8, v219
	v_cmp_lt_i32_e32 vcc, v4, v2
	s_lshl_b32 s14, s5, 3
	s_ashr_i32 s5, s4, 31
	v_cndmask_b32_e32 v4, v219, v4, vcc
	v_lshlrev_b32_e32 v107, 2, v4
	v_xor_b32_e32 v4, 16, v219
	v_cmp_lt_i32_e32 vcc, v4, v2
	s_nop 1
	v_cndmask_b32_e32 v4, v219, v4, vcc
	v_lshlrev_b32_e32 v108, 2, v4
	v_xor_b32_e32 v4, 32, v219
	v_cmp_lt_i32_e32 vcc, v4, v2
	s_nop 1
	v_cndmask_b32_e32 v2, v219, v4, vcc
	v_lshlrev_b32_e32 v109, 2, v2
	v_lshlrev_b32_e32 v2, 4, v102
	v_lshl_add_u64 v[4:5], s[6:7], 0, v[2:3]
	v_lshl_add_u64 v[16:17], v[4:5], 0, s[20:21]
	s_mov_b64 s[20:21], 0x37e00000
	v_lshl_add_u64 v[18:19], v[4:5], 0, s[20:21]
	s_lshl_b64 s[20:21], s[4:5], 12
	s_add_u32 s6, s6, s20
	s_addc_u32 s7, s7, s21
	v_lshl_add_u64 v[4:5], s[6:7], 0, v[2:3]
	s_mov_b64 s[6:7], 0x3be00000
	v_lshlrev_b32_e32 v2, 5, v102
	s_lshl_b64 s[18:19], s[18:19], 2
	v_lshl_add_u64 v[20:21], v[4:5], 0, s[6:7]
	v_or_b32_e32 v4, s18, v2
	v_mov_b32_e32 v5, s19
	v_readlane_b32 s18, v242, 3
	s_ashr_i32 s15, s14, 31
	v_readlane_b32 s19, v242, 4
	s_lshl_b64 s[6:7], s[14:15], 12
	s_nop 0
	v_lshl_add_u64 v[22:23], s[18:19], 0, v[4:5]
	s_lshl_b64 s[18:19], s[4:5], 13
	s_add_u32 s16, s16, s18
	s_addc_u32 s17, s17, s19
	v_readlane_b32 s18, v242, 5
	v_readlane_b32 s19, v242, 6
	v_lshl_add_u64 v[24:25], s[16:17], 0, v[2:3]
	s_lshl_b64 s[16:17], s[14:15], 13
	v_lshl_add_u64 v[26:27], s[18:19], 0, v[4:5]
	s_lshl_b32 s98, s36, 13
	v_lshl_add_u32 v170, v0, 4, s98
	v_readlane_b32 s18, v242, 3
	v_readlane_b32 s19, v242, 4
	v_lshlrev_b32_e32 v171, 4, v0
	v_add_u32_e32 v171, 0x10000, v171
	s_nop 4
	global_load_dwordx4 v[174:177], v170, s[18:19] offset:-16
	v_readlane_b32 s18, v242, 5
	v_readlane_b32 s19, v242, 6
	s_nop 5
	global_load_dwordx4 v[178:181], v170, s[18:19] offset:-16
	s_waitcnt vmcnt(1)
	ds_write_b128 v171, v[174:177]
	s_waitcnt vmcnt(0)
	ds_write_b128 v171, v[178:181] offset:8192
	s_waitcnt lgkmcnt(0)
	s_barrier
	s_branch .LBB0_2906

.LBB0_2911:
	v_add_u32_e32 v7, s4, v103
	ds_read_b128 v[8:11], v7
	ds_read_b128 v[28:31], v7 offset:16
	s_addk_i32 s4, 0x800
	s_cmpk_eq_i32 s4, 0x2000
	s_waitcnt lgkmcnt(1)
	v_sub_f32_e32 v12, v11, v5
	v_sub_f32_e32 v32, v9, v1
	s_waitcnt lgkmcnt(0)
	v_sub_f32_e32 v13, v31, v5
	v_sub_f32_e32 v33, v29, v1
	v_sub_f32_e32 v10, v10, v4
	v_sub_f32_e32 v8, v8, v2
	v_sub_f32_e32 v11, v30, v4
	v_sub_f32_e32 v9, v28, v2
	v_pk_mul_f32 v[28:29], v[32:33], v[32:33]
	v_pk_mul_f32 v[12:13], v[12:13], v[12:13]
	v_pk_fma_f32 v[8:9], v[8:9], v[8:9], v[28:29]
	v_pk_fma_f32 v[10:11], v[10:11], v[10:11], v[12:13]
	s_nop 0
	v_pk_add_f32 v[8:9], v[8:9], v[10:11]
	s_nop 0
	v_add_f32_e32 v7, v8, v9
	v_add_f32_e32 v6, v6, v7
	s_cbranch_scc0 .LBB0_2911
	ds_bpermute_b32 v7, v104, v6
	v_mov_b64_e32 v[32:33], v[20:21]
	v_mov_b32_e32 v34, v103
	v_lshlrev_b32_e32 v172, 5, v102
	v_add_u32_e32 v172, 0x10000, v172
	s_waitcnt lgkmcnt(0)
	v_add_f32_e32 v6, v6, v7
	ds_bpermute_b32 v7, v105, v6
	s_waitcnt lgkmcnt(0)
	v_add_f32_e32 v6, v6, v7
	ds_bpermute_b32 v7, v106, v6
	s_waitcnt lgkmcnt(0)
	v_add_f32_e32 v6, v6, v7
	ds_bpermute_b32 v7, v107, v6
	s_waitcnt lgkmcnt(0)
	v_add_f32_e32 v6, v6, v7
	ds_bpermute_b32 v7, v108, v6
	s_waitcnt lgkmcnt(0)
	v_add_f32_e32 v6, v6, v7
	ds_bpermute_b32 v7, v109, v6
	s_waitcnt lgkmcnt(0)
	v_add_f32_e32 v6, v6, v7
	v_fmamk_f32 v6, v6, 0x3a000000, v217
	v_cmp_gt_f32_e32 vcc, s87, v6
	v_mul_f32_e32 v7, 0x4f800000, v6
	s_nop 0
	v_cndmask_b32_e32 v6, v6, v7, vcc
	v_sqrt_f32_e32 v7, v6
	s_nop 0
	v_add_u32_e32 v8, -1, v7
	v_fma_f32 v9, -v8, v7, v6
	v_cmp_ge_f32_e64 s[4:5], 0, v9
	v_add_u32_e32 v9, 1, v7
	s_nop 0
	v_cndmask_b32_e64 v8, v7, v8, s[4:5]
	v_fma_f32 v7, -v9, v7, v6
	v_cmp_lt_f32_e64 s[4:5], 0, v7
	s_nop 1
	v_cndmask_b32_e64 v7, v8, v9, s[4:5]
	v_mul_f32_e32 v8, 0x37800000, v7
	v_cndmask_b32_e32 v7, v7, v8, vcc
	v_cmp_class_f32_e32 vcc, v6, v218
	s_nop 1
	v_cndmask_b32_e32 v6, v7, v6, vcc
	v_div_scale_f32 v7, s[4:5], v6, v6, 1.0
	v_rcp_f32_e32 v8, v7
	s_mov_b64 s[4:5], 0
	v_fma_f32 v9, -v7, v8, 1.0
	v_fmac_f32_e32 v8, v9, v8
	v_div_scale_f32 v9, vcc, 1.0, v6, 1.0
	v_mul_f32_e32 v10, v9, v8
	v_fma_f32 v11, -v7, v10, v9
	v_fmac_f32_e32 v10, v11, v8
	v_fma_f32 v7, -v7, v10, v9
	v_div_fmas_f32 v7, v7, v8, v10
	v_div_fixup_f32 v28, v7, v6, 1.0
	v_mov_b32_e32 v29, v28
	v_mov_b32_e32 v30, v28
	v_mov_b32_e32 v31, v28
	s_branch .LBB0_2915

.LBB0_2914:
	s_add_u32 s4, s4, 0x800
	s_addc_u32 s5, s5, 0
	s_mov_b64 s[20:21], 0x400
	v_add_u32_e32 v34, 0x800, v34
	v_add_u32_e32 v172, 0x800, v172
	s_cmpk_eq_i32 s4, 0x2000
	v_lshl_add_u64 v[32:33], v[32:33], 0, s[20:21]
	s_cbranch_scc1 .LBB0_2905
.LBB0_2915:
	ds_read_b128 v[6:9], v172 offset:8192
	ds_read_b128 v[10:13], v172
	ds_read_b128 v[36:39], v172 offset:16
	ds_read_b128 v[40:43], v172 offset:8208
	ds_read_b128 v[44:47], v34
	ds_read_b128 v[48:51], v34 offset:16
	s_andn2_b64 vcc, exec, s[12:13]
	s_waitcnt lgkmcnt(0)
	v_sub_f32_e32 v47, v47, v5
	v_sub_f32_e32 v46, v46, v4
	v_sub_f32_e32 v45, v45, v1
	v_sub_f32_e32 v44, v44, v2
	s_waitcnt lgkmcnt(0)
	v_sub_f32_e32 v51, v51, v5
	v_sub_f32_e32 v50, v50, v4
	v_sub_f32_e32 v49, v49, v1
	v_sub_f32_e32 v48, v48, v2
	v_pk_mul_f32 v[44:45], v[28:29], v[44:45]
	v_pk_mul_f32 v[46:47], v[30:31], v[46:47]
	v_pk_mul_f32 v[48:49], v[28:29], v[48:49]
	v_pk_mul_f32 v[50:51], v[30:31], v[50:51]
	v_pk_fma_f32 v[12:13], v[46:47], v[12:13], v[8:9]
	v_pk_fma_f32 v[10:11], v[44:45], v[10:11], v[6:7]
	v_pk_fma_f32 v[8:9], v[50:51], v[38:39], v[42:43]
	v_pk_fma_f32 v[6:7], v[48:49], v[36:37], v[40:41]
	s_cbranch_vccnz .LBB0_2917
	v_lshl_add_u64 v[36:37], v[24:25], 0, s[4:5]
	global_store_dwordx4 v[36:37], v[10:13], off
	global_store_dwordx4 v[36:37], v[6:9], off offset:16
	s_cbranch_execnz .LBB0_2914
	s_branch .LBB0_2913
